# LN1 row loop: the cached modulation vectors for the next row are re-loaded mid-row (after their last use) instead of at the top of the row that needs them; body vmcnt waits dropped
# baseline (speedup 1.0000x reference)
; #define GAS __attribute__((address_space(1)))
; __device__ __forceinline__ void unpack8(const u32x4 q, float* o) { o[0] = bflo(q.x); o[1] = bfhi(q.x); o[2] = bflo(q.y); o[3] = bfhi(q.y); o[4] = bflo(q.z); o[5] = bfhi(q.z); o[6] = bflo(q.w); o[7] = bfhi(q.w); }
; __device__ __forceinline__ void ph_ln1(Frame& F, int l, int ntok) {
;     ...
;         const u32x4 xa = __builtin_nontemporal_load((const GAS u32x4*)(xr + cA)), xb = __builtin_nontemporal_load((const GAS u32x4*)(xr + cA + 128)), ya = __builtin_nontemporal_load((const GAS u32x4*)yr);
;         float x[16], y[16], v[16]; unpack8(xa, x); unpack8(xb, x + 8);
;         { const unsigned a[4] = {ya.x, ya.y, ya.z, ya.w};
; #pragma unroll
;           for (int e = 0; e < 4; ++e) { const f32x2 lo = __builtin_amdgcn_cvt_pk_f32_fp8((int)a[e], false), hi = __builtin_amdgcn_cvt_pk_f32_fp8((int)a[e], true); y[4 * e] = lo.x; y[4 * e + 1] = lo.y; y[4 * e + 2] = hi.x; y[4 * e + 3] = hi.y; } }
;         float s = 0.f;
; #pragma unroll
;         for (int j = 0; j < 4; ++j) { const f32x4 g1 = *(const GAS f32x4*)(md + 2048 + LN1_COL(j));
; #pragma unroll
;             for (int e = 0; e < 4; ++e) { v[4 * j + e] = x[4 * j + e] * DN_ALPHA + g1[e] * y[4 * j + e]; s += v[4 * j + e]; } }
;         const float mean = wave_sum(s, F.lane) * (1.f / DM); float s2 = 0.f;
; #pragma unroll
;         for (int e = 0; e < 16; ++e) { v[e] -= mean; s2 += v[e] * v[e]; }
;         const float rstd = 1.f / sqrtf(wave_sum(s2, F.lane) * (1.f / DM) + LN_EPS);
;         unsigned wx[8]; int w8[4];
; #pragma unroll
;         for (int j = 0; j < 4; ++j) { const f32x4 g = *(const GAS f32x4*)(lg + LN1_COL(j)), bb = *(const GAS f32x4*)(lb + LN1_COL(j)), sh = *(const GAS f32x4*)(md + 3072 + LN1_COL(j)), sc = *(const GAS f32x4*)(md + 4096 + LN1_COL(j));
.Lln1_md_keep:
	s_waitcnt vmcnt(0)
	v_mov_b32_e32 v46, v128
	v_mov_b32_e32 v47, v129
	v_mov_b32_e32 v48, v130
	v_mov_b32_e32 v49, v131
	v_mov_b32_e32 v90, v132
	v_mov_b32_e32 v91, v133
	v_mov_b32_e32 v92, v134
	v_mov_b32_e32 v93, v135
	v_mov_b32_e32 v0, v144
	v_mov_b32_e32 v1, v145
	v_mov_b32_e32 v2, v146
	v_mov_b32_e32 v3, v147
	s_add_i32 s87, s40, s8
	s_cmp_lt_i32 s87, s80
	s_cselect_b64 s[86:87], -1, 0
	v_lshl_add_u64 v[148:149], s[38:39], 0, v[62:63]
	v_lshl_add_u64 v[148:149], v[148:149], 0, s[84:85]
	v_lshl_add_u64 v[150:151], s[38:39], 0, v[64:65]
	v_cndmask_b32_e64 v148, v68, v148, s[86:87]
	v_cndmask_b32_e64 v149, v69, v149, s[86:87]
	v_cndmask_b32_e64 v150, v68, v150, s[86:87]
	v_cndmask_b32_e64 v151, v69, v151, s[86:87]
	global_load_dwordx4 v[128:131], v[148:149], off nt
	global_load_dwordx4 v[132:135], v[148:149], off offset:256 nt
	global_load_dwordx4 v[144:147], v[150:151], off nt
	v_lshlrev_b32_e32 v122, 16, v93
	v_cvt_pk_f32_fp8_e32 v[24:25], v0
	v_cvt_pk_f32_fp8_sdwa v[70:71], v0 src0_sel:WORD_1
	v_cvt_pk_f32_fp8_e32 v[72:73], v1
	v_cvt_pk_f32_fp8_sdwa v[74:75], v1 src0_sel:WORD_1
	v_lshl_add_u64 v[0:1], s[2:3], 0, v[54:55]
	v_mov_b32_e32 v50, v136
	v_mov_b32_e32 v51, v137
	v_mov_b32_e32 v52, v138
	v_mov_b32_e32 v53, v139
	v_mov_b32_e32 v94, v140
	v_mov_b32_e32 v95, v141
	v_mov_b32_e32 v96, v142
	v_mov_b32_e32 v97, v143
	v_lshl_add_u64 v[0:1], s[2:3], 0, v[66:67]
	v_mov_b32_e32 v98, v152
	v_mov_b32_e32 v99, v153
	v_mov_b32_e32 v100, v154
	v_mov_b32_e32 v101, v155
	v_mov_b32_e32 v102, v188
	v_mov_b32_e32 v103, v189
	v_mov_b32_e32 v104, v190
	v_mov_b32_e32 v105, v191
	s_add_u32 s2, s0, 0x4000
	s_addc_u32 s3, s4, 0
	v_lshl_add_u64 v[0:1], s[36:37], 0, v[54:55]
	v_lshl_add_u64 v[4:5], s[2:3], 0, v[54:55]
	v_cvt_pk_f32_fp8_e32 v[114:115], v2
	v_cvt_pk_f32_fp8_sdwa v[116:117], v2 src0_sel:WORD_1
	v_cvt_pk_f32_fp8_e32 v[118:119], v3
	v_cvt_pk_f32_fp8_sdwa v[120:121], v3 src0_sel:WORD_1
	v_mov_b32_e32 v26, v156
	v_mov_b32_e32 v27, v157
	v_mov_b32_e32 v28, v158
	v_mov_b32_e32 v29, v159
	v_mov_b32_e32 v106, v160
	v_mov_b32_e32 v107, v161
	v_mov_b32_e32 v108, v162
	v_mov_b32_e32 v109, v163
	v_mov_b32_e32 v30, v164
	v_mov_b32_e32 v31, v165
	v_mov_b32_e32 v32, v166
	v_mov_b32_e32 v33, v167
	v_mov_b32_e32 v110, v168
	v_mov_b32_e32 v111, v169
	v_mov_b32_e32 v112, v170
	v_mov_b32_e32 v113, v171
	v_mov_b32_e32 v12, v194
	v_mov_b32_e32 v13, v195
	v_mov_b32_e32 v14, v196
	v_mov_b32_e32 v15, v197
	v_mov_b32_e32 v42, v198
	v_mov_b32_e32 v43, v199
	v_mov_b32_e32 v44, v200
	v_mov_b32_e32 v45, v201
	s_nop 0
	v_mov_b32_e32 v0, v202
	v_mov_b32_e32 v1, v203
	v_mov_b32_e32 v2, v204
	v_mov_b32_e32 v3, v205
	s_nop 0
	v_mov_b32_e32 v4, v206
	v_mov_b32_e32 v5, v207
	v_mov_b32_e32 v6, v208
	v_mov_b32_e32 v7, v209
	v_and_b32_e32 v123, 0xffff0000, v93
	v_lshl_add_u64 v[82:83], s[2:3], 0, v[66:67]
	s_waitcnt lgkmcnt(0)
	v_mov_b32_e32 v8, v172
	v_mov_b32_e32 v9, v173
	v_mov_b32_e32 v10, v174
	v_mov_b32_e32 v11, v175
	v_mov_b32_e32 v34, v176
	v_mov_b32_e32 v35, v177
	v_mov_b32_e32 v36, v178
	v_mov_b32_e32 v37, v179
	v_mov_b32_e32 v16, v180
	v_mov_b32_e32 v17, v181
	v_mov_b32_e32 v18, v182
	v_mov_b32_e32 v19, v183
	v_mov_b32_e32 v38, v184
	v_mov_b32_e32 v39, v185
	v_mov_b32_e32 v40, v186
	v_mov_b32_e32 v41, v187
	s_mov_b32 s0, 0x5be00000
	s_add_i32 s40, s40, s8
	s_cmp_lt_i32 s40, s80
	v_pk_mul_f32 v[52:53], v[70:71], v[52:53]
	v_lshlrev_b32_e32 v70, 16, v46
	v_and_b32_e32 v71, 0xffff0000, v46
	v_pk_mul_f32 v[24:25], v[24:25], v[50:51]
	v_pk_mul_f32 v[104:105], v[120:121], v[104:105]
	v_lshlrev_b32_e32 v120, 16, v92
	v_and_b32_e32 v121, 0xffff0000, v92
	v_pk_mul_f32 v[92:93], v[118:119], v[102:103]
	v_lshlrev_b32_e32 v102, 16, v91
	v_and_b32_e32 v103, 0xffff0000, v91
	v_pk_mul_f32 v[100:101], v[116:117], v[100:101]
	v_pk_fma_f32 v[24:25], v[70:71], s[20:21], v[24:25] op_sel_hi:[1,0,1]
	v_pk_fma_f32 v[100:101], v[102:103], s[20:21], v[100:101] op_sel_hi:[1,0,1]
	v_lshlrev_b32_e32 v102, 16, v90
	v_and_b32_e32 v103, 0xffff0000, v90
	v_pk_mul_f32 v[90:91], v[114:115], v[98:99]
	v_lshlrev_b32_e32 v98, 16, v49
	v_and_b32_e32 v99, 0xffff0000, v49
	v_pk_mul_f32 v[74:75], v[74:75], v[96:97]
	v_lshlrev_b32_e32 v96, 16, v48
	v_and_b32_e32 v97, 0xffff0000, v48
	v_pk_mul_f32 v[48:49], v[72:73], v[94:95]
	v_lshlrev_b32_e32 v72, 16, v47
	v_and_b32_e32 v73, 0xffff0000, v47
	v_add_f32_e32 v46, 0, v24
	v_pk_fma_f32 v[52:53], v[72:73], s[20:21], v[52:53] op_sel_hi:[1,0,1]
	v_add_f32_e32 v46, v25, v46
	v_add_f32_e32 v46, v52, v46
	v_pk_fma_f32 v[48:49], v[96:97], s[20:21], v[48:49] op_sel_hi:[1,0,1]
	v_add_f32_e32 v46, v53, v46
	v_add_f32_e32 v46, v48, v46
	v_pk_fma_f32 v[74:75], v[98:99], s[20:21], v[74:75] op_sel_hi:[1,0,1]
	v_add_f32_e32 v46, v49, v46
	v_add_f32_e32 v46, v74, v46
	v_pk_fma_f32 v[90:91], v[102:103], s[20:21], v[90:91] op_sel_hi:[1,0,1]
	v_add_f32_e32 v46, v75, v46
	v_add_f32_e32 v46, v90, v46
	v_add_f32_e32 v46, v91, v46
	v_add_f32_e32 v46, v100, v46
	v_pk_fma_f32 v[92:93], v[120:121], s[20:21], v[92:93] op_sel_hi:[1,0,1]
	v_add_f32_e32 v46, v101, v46
	v_add_f32_e32 v46, v92, v46
	v_pk_fma_f32 v[104:105], v[122:123], s[20:21], v[104:105] op_sel_hi:[1,0,1]
	v_add_f32_e32 v46, v93, v46
	v_add_f32_e32 v46, v104, v46
	v_add_f32_e32 v46, v105, v46
	ds_bpermute_b32 v47, v76, v46
	v_add_f32_e32 v124, 1.0, v4
	v_add_f32_e32 v125, 1.0, v5
	v_lshl_add_u64 v[4:5], s[36:37], 0, v[66:67]
	v_add_f32_e32 v126, 1.0, v6
	s_waitcnt lgkmcnt(0)
	v_add_f32_e32 v46, v46, v47
	ds_bpermute_b32 v47, v77, v46
	v_add_f32_e32 v127, 1.0, v7
	v_add_f32_e32 v86, 1.0, v0
	v_add_f32_e32 v87, 1.0, v1
	v_add_f32_e32 v88, 1.0, v2
	s_waitcnt lgkmcnt(0)
	v_add_f32_e32 v46, v46, v47
	ds_bpermute_b32 v47, v78, v46
	v_add_f32_e32 v89, 1.0, v3
	v_mov_b32_e32 v0, v210
	v_mov_b32_e32 v1, v211
	v_mov_b32_e32 v2, v212
	v_mov_b32_e32 v3, v213
	v_mov_b32_e32 v20, v214
	v_mov_b32_e32 v21, v215
	v_mov_b32_e32 v22, v216
	v_mov_b32_e32 v23, v217
	s_nop 0
	v_mov_b32_e32 v4, v218
	v_mov_b32_e32 v5, v219
	v_mov_b32_e32 v6, v220
	v_mov_b32_e32 v7, v221
	s_nop 0
	v_mov_b32_e32 v82, v222
	v_mov_b32_e32 v83, v223
	v_mov_b32_e32 v84, v224
	v_mov_b32_e32 v85, v225
	s_cselect_b32 s89, 1, 0
	s_min_i32 s86, s40, 0x10000
	s_ashr_i32 s86, s86, 12
	s_mul_i32 s87, s30, 17
	s_add_i32 s86, s86, s87
	s_mul_hi_u32 s87, s86, 0x6000
	s_mul_i32 s86, s86, 0x6000
	s_add_u32 s86, s22, s86
	s_addc_u32 s87, s42, s87
	s_cmp_eq_u32 s86, s88
	s_cbranch_scc1 .Lln1_md_next_keep
; #define GAS __attribute__((address_space(1)))
; __device__ __forceinline__ void ph_ln1(Frame& F, int l, int ntok) {
;     ...
;         for (int j = 0; j < 4; ++j) { const f32x4 g1 = *(const GAS f32x4*)(md + 2048 + LN1_COL(j));
; #pragma unroll
;             for (int e = 0; e < 4; ++e) { v[4 * j + e] = x[4 * j + e] * DN_ALPHA + g1[e] * y[4 * j + e]; s += v[4 * j + e]; } }
;         const float mean = wave_sum(s, F.lane) * (1.f / DM); float s2 = 0.f;
; #pragma unroll
;         for (int e = 0; e < 16; ++e) { v[e] -= mean; s2 += v[e] * v[e]; }
;         const float rstd = 1.f / sqrtf(wave_sum(s2, F.lane) * (1.f / DM) + LN_EPS);
;         unsigned wx[8]; int w8[4];
; #pragma unroll
;         for (int j = 0; j < 4; ++j) { const f32x4 g = *(const GAS f32x4*)(lg + LN1_COL(j)), bb = *(const GAS f32x4*)(lb + LN1_COL(j)), sh = *(const GAS f32x4*)(md + 3072 + LN1_COL(j)), sc = *(const GAS f32x4*)(md + 4096 + LN1_COL(j));
	s_mov_b32 s88, s86
	s_add_u32 s90, s86, 0x2000
	s_addc_u32 s91, s87, 0
	v_lshl_add_u64 v[236:237], s[90:91], 0, v[54:55]
	s_add_u32 s90, s86, 0x2000
	s_addc_u32 s91, s87, 0
	v_lshl_add_u64 v[238:239], s[90:91], 0, v[66:67]
	s_add_u32 s90, s86, 0x3000
	s_addc_u32 s91, s87, 0
	v_lshl_add_u64 v[240:241], s[90:91], 0, v[54:55]
	s_add_u32 s90, s86, 0x3000
	s_addc_u32 s91, s87, 0
	v_lshl_add_u64 v[242:243], s[90:91], 0, v[66:67]
	s_add_u32 s90, s86, 0x4000
	s_addc_u32 s91, s87, 0
	v_lshl_add_u64 v[244:245], s[90:91], 0, v[54:55]
	s_add_u32 s90, s86, 0x4000
	s_addc_u32 s91, s87, 0
	v_lshl_add_u64 v[246:247], s[90:91], 0, v[66:67]
	global_load_dwordx4 v[136:139], v[236:237], off
	global_load_dwordx4 v[140:143], v[236:237], off offset:16
	global_load_dwordx4 v[152:155], v[238:239], off
	global_load_dwordx4 v[188:191], v[238:239], off offset:16
	global_load_dwordx4 v[194:197], v[240:241], off offset:16
	global_load_dwordx4 v[198:201], v[240:241], off
	global_load_dwordx4 v[202:205], v[244:245], off offset:16
	global_load_dwordx4 v[206:209], v[244:245], off
	global_load_dwordx4 v[210:213], v[242:243], off offset:16
	global_load_dwordx4 v[214:217], v[242:243], off
	global_load_dwordx4 v[218:221], v[246:247], off offset:16
	global_load_dwordx4 v[222:225], v[246:247], off
; #define GAS __attribute__((address_space(1)))
; __device__ __forceinline__ unsigned pk2(float lo, float hi) { const f32x2 v = {lo, hi}; const bf16v2 b = __builtin_convertvector(v, bf16v2); return __builtin_bit_cast(unsigned, b); }
; __device__ __forceinline__ void ph_ln1(Frame& F, int l, int ntok) {
;     ...
;         const float mean = wave_sum(s, F.lane) * (1.f / DM); float s2 = 0.f;
; #pragma unroll
;         for (int e = 0; e < 16; ++e) { v[e] -= mean; s2 += v[e] * v[e]; }
;         const float rstd = 1.f / sqrtf(wave_sum(s2, F.lane) * (1.f / DM) + LN_EPS);
;         unsigned wx[8]; int w8[4];
; #pragma unroll
;         for (int j = 0; j < 4; ++j) { const f32x4 g = *(const GAS f32x4*)(lg + LN1_COL(j)), bb = *(const GAS f32x4*)(lb + LN1_COL(j)), sh = *(const GAS f32x4*)(md + 3072 + LN1_COL(j)), sc = *(const GAS f32x4*)(md + 4096 + LN1_COL(j));
;             float xn[4];
; #pragma unroll
;             for (int e = 0; e < 4; ++e) xn[e] = v[4 * j + e] * rstd * g[e] + bb[e];
;             wx[2 * j] = pk2(xn[0], xn[1]); wx[2 * j + 1] = pk2(xn[2], xn[3]);
;             const float h0 = xn[0] * (1.f + sc[0]) + sh[0], h1 = xn[1] * (1.f + sc[1]) + sh[1], h2 = xn[2] * (1.f + sc[2]) + sh[2], h3 = xn[3] * (1.f + sc[3]) + sh[3];
;             int v = 0; v = __builtin_amdgcn_cvt_pk_fp8_f32(h0, h1, v, false); v = __builtin_amdgcn_cvt_pk_fp8_f32(h2, h3, v, true); w8[j] = v; }
;         unsigned char* x8 = (unsigned char*)(F.ws + WS_XM8) + (size_t)row * DM;
;         __builtin_nontemporal_store((u32x2){(unsigned)w8[0], (unsigned)w8[1]}, (GAS u32x2*)(x8 + cA)); __builtin_nontemporal_store((u32x2){(unsigned)w8[2], (unsigned)w8[3]}, (GAS u32x2*)(x8 + cA + 128));
;         __builtin_nontemporal_store((u32x4){wx[0], wx[1], wx[2], wx[3]}, (GAS u32x4*)(xr + cA)); __builtin_nontemporal_store((u32x4){wx[4], wx[5], wx[6], wx[7]}, (GAS u32x4*)(xr + cA + 128));
.Lln1_md_next_keep:
	s_cmp_lg_u32 s89, 0
	s_waitcnt lgkmcnt(0)
	v_add_f32_e32 v46, v46, v47
	ds_bpermute_b32 v47, v79, v46
	s_waitcnt lgkmcnt(0)
	v_add_f32_e32 v46, v46, v47
	ds_bpermute_b32 v47, v80, v46
	s_waitcnt lgkmcnt(0)
	v_add_f32_e32 v46, v46, v47
	ds_bpermute_b32 v47, v81, v46
	s_waitcnt lgkmcnt(0)
	v_add_f32_e32 v46, v46, v47
	v_mul_f32_e32 v50, 0x3a800000, v46
	v_pk_add_f32 v[24:25], v[24:25], v[50:51] op_sel_hi:[1,0] neg_lo:[0,1] neg_hi:[0,1]
	v_pk_add_f32 v[96:97], v[52:53], v[50:51] op_sel_hi:[1,0] neg_lo:[0,1] neg_hi:[0,1]
	v_pk_mul_f32 v[94:95], v[24:25], v[24:25]
	v_pk_mul_f32 v[98:99], v[96:97], v[96:97]
	v_add_f32_e32 v94, v94, v95
	v_pk_add_f32 v[72:73], v[48:49], v[50:51] op_sel_hi:[1,0] neg_lo:[0,1] neg_hi:[0,1]
	v_add_f32_e32 v94, v98, v94
	v_pk_mul_f32 v[102:103], v[72:73], v[72:73]
	v_add_f32_e32 v94, v99, v94
	v_pk_add_f32 v[74:75], v[74:75], v[50:51] op_sel_hi:[1,0] neg_lo:[0,1] neg_hi:[0,1]
	v_add_f32_e32 v94, v102, v94
	v_pk_mul_f32 v[114:115], v[74:75], v[74:75]
	v_add_f32_e32 v94, v103, v94
	v_pk_add_f32 v[52:53], v[90:91], v[50:51] op_sel_hi:[1,0] neg_lo:[0,1] neg_hi:[0,1]
	v_add_f32_e32 v94, v114, v94
	v_pk_mul_f32 v[90:91], v[52:53], v[52:53]
	v_add_f32_e32 v94, v115, v94
	v_pk_add_f32 v[70:71], v[100:101], v[50:51] op_sel_hi:[1,0] neg_lo:[0,1] neg_hi:[0,1]
	v_add_f32_e32 v90, v90, v94
	v_pk_mul_f32 v[100:101], v[70:71], v[70:71]
	v_add_f32_e32 v90, v91, v90
	v_pk_add_f32 v[46:47], v[92:93], v[50:51] op_sel_hi:[1,0] neg_lo:[0,1] neg_hi:[0,1]
	v_add_f32_e32 v90, v100, v90
	v_pk_mul_f32 v[92:93], v[46:47], v[46:47]
	v_add_f32_e32 v90, v101, v90
	v_pk_add_f32 v[48:49], v[104:105], v[50:51] op_sel_hi:[1,0] neg_lo:[0,1] neg_hi:[0,1]
	v_add_f32_e32 v90, v92, v90
	v_pk_mul_f32 v[50:51], v[48:49], v[48:49]
	v_add_f32_e32 v90, v93, v90
	v_add_f32_e32 v50, v50, v90
	v_add_f32_e32 v50, v51, v50
	ds_bpermute_b32 v51, v76, v50
	s_waitcnt lgkmcnt(0)
	v_add_f32_e32 v50, v50, v51
	ds_bpermute_b32 v51, v77, v50
	s_waitcnt lgkmcnt(0)
	v_add_f32_e32 v50, v50, v51
	ds_bpermute_b32 v51, v78, v50
	s_waitcnt lgkmcnt(0)
	v_add_f32_e32 v50, v50, v51
	ds_bpermute_b32 v51, v79, v50
	s_waitcnt lgkmcnt(0)
	v_add_f32_e32 v50, v50, v51
	ds_bpermute_b32 v51, v80, v50
	v_add_f32_e32 v4, 1.0, v4
	v_add_f32_e32 v82, 1.0, v82
	v_add_f32_e32 v83, 1.0, v83
	s_waitcnt lgkmcnt(0)
	v_add_f32_e32 v50, v50, v51
	ds_bpermute_b32 v51, v81, v50
	v_add_f32_e32 v84, 1.0, v84
	v_add_f32_e32 v85, 1.0, v85
	s_waitcnt lgkmcnt(0)
	v_add_f32_e32 v50, v50, v51
	v_fmamk_f32 v50, v50, 0x3a800000, v234
	v_cmp_gt_f32_e32 vcc, s9, v50
	v_mul_f32_e32 v51, 0x4f800000, v50
	s_nop 0
	v_cndmask_b32_e32 v50, v50, v51, vcc
	v_sqrt_f32_e32 v51, v50
	s_nop 0
	v_add_u32_e32 v90, -1, v51
	v_fma_f32 v91, -v90, v51, v50
	v_cmp_ge_f32_e64 s[36:37], 0, v91
	v_add_u32_e32 v91, 1, v51
	s_nop 0
	v_cndmask_b32_e64 v90, v51, v90, s[36:37]
	v_fma_f32 v51, -v91, v51, v50
	v_cmp_lt_f32_e64 s[36:37], 0, v51
	s_nop 1
	v_cndmask_b32_e64 v51, v90, v91, s[36:37]
	v_mul_f32_e32 v90, 0x37800000, v51
	v_cndmask_b32_e32 v51, v51, v90, vcc
	v_cmp_class_f32_e32 vcc, v50, v232
	s_nop 1
	v_cndmask_b32_e32 v50, v51, v50, vcc
	v_div_scale_f32 v51, s[2:3], v50, v50, 1.0
	v_rcp_f32_e32 v90, v51
	s_nop 0
	v_fma_f32 v91, -v51, v90, 1.0
	v_fmac_f32_e32 v90, v91, v90
	v_div_scale_f32 v91, vcc, 1.0, v50, 1.0
	v_mul_f32_e32 v92, v91, v90
	v_fma_f32 v93, -v51, v92, v91
	v_fmac_f32_e32 v92, v93, v90
	v_fma_f32 v51, -v51, v92, v91
	v_div_fmas_f32 v51, v51, v90, v92
	v_div_fixup_f32 v50, v51, v50, 1.0
	v_pk_mul_f32 v[24:25], v[24:25], v[50:51] op_sel_hi:[1,0]
	s_nop 0
	v_pk_fma_f32 v[90:91], v[106:107], v[24:25], v[110:111]
	v_pk_mul_f32 v[24:25], v[96:97], v[50:51] op_sel_hi:[1,0]
	v_fma_f32 v42, v124, v90, v42
	v_pk_fma_f32 v[92:93], v[108:109], v[24:25], v[112:113]
	v_cvt_pk_bf16_f32 v24, v90, v91
	v_fma_f32 v43, v125, v91, v43
	v_mov_b32_e32 v90, v193
	v_cvt_pk_fp8_f32 v90, v42, v43
	v_pk_mul_f32 v[42:43], v[72:73], v[50:51] op_sel_hi:[1,0]
	v_mov_b32_e32 v91, v193
	v_pk_fma_f32 v[30:31], v[26:27], v[42:43], v[30:31]
	v_pk_mul_f32 v[26:27], v[74:75], v[50:51] op_sel_hi:[1,0]
	v_fma_f32 v12, v86, v30, v12
	v_fma_f32 v13, v87, v31, v13
	v_cvt_pk_fp8_f32 v91, v12, v13
	v_pk_fma_f32 v[28:29], v[28:29], v[26:27], v[32:33]
	v_pk_mul_f32 v[12:13], v[52:53], v[50:51] op_sel_hi:[1,0]
	v_fma_f32 v14, v88, v28, v14
	v_fmac_f32_e32 v15, v89, v29
	v_cvt_pk_fp8_f32 v91, v14, v15 op_sel:[0,0,1]
	v_pk_fma_f32 v[14:15], v[34:35], v[12:13], v[38:39]
	v_pk_mul_f32 v[12:13], v[70:71], v[50:51] op_sel_hi:[1,0]
	v_cvt_pk_bf16_f32 v27, v28, v29
	v_pk_fma_f32 v[28:29], v[36:37], v[12:13], v[40:41]
	v_cvt_pk_bf16_f32 v12, v14, v15
	v_fma_f32 v14, v82, v14, v20
	v_fma_f32 v15, v83, v15, v21
	v_mov_b32_e32 v20, v193
	v_cvt_pk_fp8_f32 v20, v14, v15
	v_pk_mul_f32 v[14:15], v[46:47], v[50:51] op_sel_hi:[1,0]
	v_fma_f32 v21, v84, v28, v22
	v_pk_fma_f32 v[8:9], v[8:9], v[14:15], v[16:17]
	v_fmac_f32_e32 v23, v85, v29
	v_fma_f32 v0, v4, v8, v0
	v_add_f32_e32 v4, 1.0, v5
	v_cvt_pk_fp8_f32 v20, v21, v23 op_sel:[0,0,1]
	v_fma_f32 v1, v4, v9, v1
	v_mov_b32_e32 v21, v193
	v_pk_mul_f32 v[14:15], v[48:49], v[50:51] op_sel_hi:[1,0]
	v_cvt_pk_fp8_f32 v21, v0, v1
	v_pk_fma_f32 v[10:11], v[10:11], v[14:15], v[18:19]
	v_add_f32_e32 v4, 1.0, v6
	v_fma_f32 v44, v126, v92, v44
	v_fmac_f32_e32 v45, v127, v93
	v_fma_f32 v2, v4, v10, v2
	v_add_f32_e32 v4, 1.0, v7
	v_cvt_pk_fp8_f32 v90, v44, v45 op_sel:[0,0,1]
	v_fmac_f32_e32 v3, v4, v11
	v_cvt_pk_fp8_f32 v21, v2, v3 op_sel:[0,0,1]
	v_lshl_add_u64 v[0:1], s[38:39], 0, v[60:61]
	v_add_co_u32_e32 v0, vcc, s0, v0
	v_lshl_add_u64 v[60:61], v[60:61], 0, s[10:11]
	s_nop 0
	v_addc_co_u32_e32 v1, vcc, 0, v1, vcc
	v_cvt_pk_bf16_f32 v25, v92, v93
	v_cvt_pk_bf16_f32 v26, v30, v31
	v_cvt_pk_bf16_f32 v13, v28, v29
	v_cvt_pk_bf16_f32 v14, v8, v9
	v_cvt_pk_bf16_f32 v15, v10, v11
	global_store_dwordx2 v[0:1], v[90:91], off nt
	global_store_dwordx2 v[0:1], v[20:21], off offset:128 nt
	global_store_dwordx4 v[68:69], v[24:27], off nt
	global_store_dwordx4 v[68:69], v[12:15], off offset:256 nt
	s_cbranch_scc1 .LBB0_775
